# h1 barrier split by tile halves: only first-half h1 stores gate the first barrier, second barrier mid layer-1; per-wave k-step order regrouped (even k-steps then odd)
# speedup vs baseline: 1.0034x; 1.0003x over previous
_Z16pdag_main_kernelPKfS0_S0_PKDv8_DF16_S3_S0_PKDF16_S5_S0_Pf:
	s_load_dwordx8 s[4:11], s[0:1], 0x0
	s_load_dwordx8 s[12:19], s[0:1], 0x20
	s_lshl_b32 s2, s2, 6
	s_ashr_i32 s3, s2, 31
	s_lshl_b64 s[24:25], s[2:3], 6
	v_mov_b32_e32 v136, 0
	s_waitcnt lgkmcnt(0)
	s_add_u32 s4, s4, s24
	s_addc_u32 s5, s5, s25
	v_lshlrev_b32_e32 v146, 2, v0
	v_lshlrev_b32_e32 v172, 4, v0
	v_mov_b32_e32 v173, v136
	global_load_dword v174, v146, s[4:5]
	global_load_dword v175, v146, s[4:5] offset:2048
	v_lshl_add_u64 v[2:3], s[14:15], 0, v[172:173]
	s_movk_i32 s4, 0x2000
	v_add_co_u32_e32 v4, vcc, s4, v2
	s_movk_i32 s5, 0x4000
	s_nop 0
	v_addc_co_u32_e32 v5, vcc, 0, v3, vcc
	v_add_co_u32_e32 v6, vcc, s5, v2
	s_movk_i32 s5, 0x6000
	s_nop 0
	v_addc_co_u32_e32 v7, vcc, 0, v3, vcc
	v_add_co_u32_e32 v2, vcc, s5, v2
	v_and_b32_e32 v1, 15, v0
	s_nop 0
	v_addc_co_u32_e32 v3, vcc, 0, v3, vcc
	global_load_dwordx4 v[148:151], v[4:5], off
	global_load_dwordx4 v[152:155], v[6:7], off
	global_load_dwordx4 v[156:159], v[2:3], off
	v_lshl_add_u64 v[2:3], s[16:17], 0, v[172:173]
	v_or_b32_e32 v10, s2, v1
	v_add_co_u32_e32 v2, vcc, s4, v2
	v_or_b32_e32 v12, 16, v10
	s_nop 0
	v_addc_co_u32_e32 v3, vcc, 0, v3, vcc
	v_ashrrev_i32_e32 v11, 31, v10
	v_mad_i64_i32 v[6:7], s[4:5], v10, 40, s[6:7]
	v_ashrrev_i32_e32 v13, 31, v12
	global_load_dwordx4 v[160:163], v172, s[14:15]
	global_load_dwordx4 v[164:167], v172, s[16:17]
	global_load_dwordx4 v[168:171], v[2:3], off
	global_load_dwordx2 v[144:145], v[6:7], off offset:32
	s_nop 0
	global_load_dwordx4 v[2:5], v[6:7], off offset:16
	global_load_dwordx4 v[126:129], v[6:7], off
	v_lshl_add_u64 v[6:7], v[10:11], 4, s[8:9]
	v_mad_i64_i32 v[14:15], s[4:5], v12, 40, s[6:7]
	v_lshl_add_u64 v[12:13], v[12:13], 4, s[8:9]
	global_load_dwordx4 v[122:125], v[6:7], off
	global_load_dwordx2 v[142:143], v[14:15], off offset:32
	s_nop 0
	global_load_dwordx4 v[6:9], v[14:15], off offset:16
	global_load_dwordx4 v[118:121], v[14:15], off
	global_load_dwordx4 v[114:117], v[12:13], off
	v_or_b32_e32 v12, 32, v10
	v_ashrrev_i32_e32 v13, 31, v12
	v_readfirstlane_b32 s22, v0
	v_mad_i64_i32 v[18:19], s[4:5], v12, 40, s[6:7]
	v_lshl_add_u64 v[12:13], v[12:13], 4, s[8:9]
	v_or_b32_e32 v10, 48, v10
	s_mov_b32 s21, 0
	s_lshr_b32 s20, s22, 6
	global_load_dwordx2 v[140:141], v[18:19], off offset:32
	global_load_dwordx4 v[14:17], v[18:19], off offset:16
	global_load_dwordx4 v[110:113], v[18:19], off
	global_load_dwordx4 v[106:109], v[12:13], off
	v_ashrrev_i32_e32 v11, 31, v10
	v_mad_i64_i32 v[12:13], s[4:5], v10, 40, s[6:7]
	v_lshl_add_u64 v[10:11], v[10:11], 4, s[8:9]
	s_lshl_b64 s[4:5], s[20:21], 16
	global_load_dwordx2 v[138:139], v[12:13], off offset:32
	global_load_dwordx4 v[26:29], v[12:13], off offset:16
	global_load_dwordx4 v[102:105], v[12:13], off
	global_load_dwordx4 v[98:101], v[10:11], off
	s_add_u32 s4, s12, s4
	v_and_b32_e32 v10, 31, v0
	s_addc_u32 s5, s13, s5
	v_lshlrev_b32_e32 v130, 4, v10
	s_lshl_b64 s[6:7], s[20:21], 7
	global_load_dwordx4 v[30:33], v130, s[4:5]
	global_load_dwordx4 v[22:25], v130, s[4:5] offset:1024
	global_load_dwordx4 v[18:21], v130, s[4:5] offset:2048
	global_load_dwordx4 v[10:13], v130, s[4:5] offset:3072
	s_add_u32 s8, s18, s6
	s_addc_u32 s9, s19, s7
	v_lshlrev_b32_e32 v132, 3, v1
	global_load_dwordx2 v[134:135], v132, s[8:9]
	s_load_dwordx4 s[12:15], s[0:1], 0x40
	v_and_b32_e32 v137, 63, v0
	v_mov_b32_e32 v131, v136
	v_mov_b32_e32 v133, v136
	v_lshlrev_b32_e32 v34, 4, v137
	s_mov_b32 s19, 0x20000
	s_mov_b32 s18, 0x880000
	s_and_b32 s17, s11, 0xffff
	s_mov_b32 s16, s10
	v_lshl_or_b32 v147, s20, 12, v34
	s_lshl_b32 s55, s20, 1
	s_lshl_b32 s56, s20, 1
	s_lshl_b32 s60, s56, 15
	s_lshl_b32 s56, s20, 1
	s_or_b32 s56, s56, 1
	s_lshl_b32 s61, s56, 15
	s_add_i32 s56, s20, 1
	s_and_b32 s56, s56, 7
	s_lshl_b32 s56, s56, 1
	s_lshl_b32 s62, s56, 15
	s_add_i32 s56, s20, 2
	s_and_b32 s56, s56, 7
	s_lshl_b32 s56, s56, 1
	s_lshl_b32 s63, s56, 15
	s_add_i32 s56, s20, 3
	s_and_b32 s56, s56, 7
	s_lshl_b32 s56, s56, 1
	s_lshl_b32 s56, s56, 15
	s_add_i32 s34, s56, 0xfff68000
	s_add_i32 s56, s20, 4
	s_and_b32 s56, s56, 7
	s_lshl_b32 s56, s56, 1
	s_lshl_b32 s56, s56, 15
	s_add_i32 s35, s56, 0xfff68000
	s_add_i32 s56, s20, 5
	s_and_b32 s56, s56, 7
	s_lshl_b32 s56, s56, 1
	s_lshl_b32 s56, s56, 15
	s_add_i32 s36, s56, 0xfff68000
	s_add_i32 s56, s20, 6
	s_and_b32 s56, s56, 7
	s_lshl_b32 s56, s56, 1
	s_lshl_b32 s56, s56, 15
	s_add_i32 s37, s56, 0xfff68000
	s_add_i32 s56, s20, 7
	s_and_b32 s56, s56, 7
	s_lshl_b32 s56, s56, 1
	s_lshl_b32 s56, s56, 15
	s_add_i32 s38, s56, 0xfff68000
	s_add_i32 s56, s20, 1
	s_and_b32 s56, s56, 7
	s_lshl_b32 s56, s56, 1
	s_or_b32 s56, s56, 1
	s_lshl_b32 s56, s56, 15
	s_add_i32 s39, s56, 0xfff68000
	s_add_i32 s56, s20, 2
	s_and_b32 s56, s56, 7
	s_lshl_b32 s56, s56, 1
	s_or_b32 s56, s56, 1
	s_lshl_b32 s56, s56, 15
	s_add_i32 s40, s56, 0xfff68000
	s_add_i32 s56, s20, 3
	s_and_b32 s56, s56, 7
	s_lshl_b32 s56, s56, 1
	s_or_b32 s56, s56, 1
	s_lshl_b32 s56, s56, 15
	s_add_i32 s41, s56, 0xfff68000
	s_add_i32 s56, s20, 4
	s_and_b32 s56, s56, 7
	s_lshl_b32 s56, s56, 1
	s_or_b32 s56, s56, 1
	s_lshl_b32 s56, s56, 15
	s_add_i32 s42, s56, 0xfff68000
	s_add_i32 s56, s20, 5
	s_and_b32 s56, s56, 7
	s_lshl_b32 s56, s56, 1
	s_or_b32 s56, s56, 1
	s_lshl_b32 s56, s56, 15
	s_add_i32 s43, s56, 0xfff68000
	s_add_i32 s56, s20, 6
	s_and_b32 s56, s56, 7
	s_lshl_b32 s56, s56, 1
	s_or_b32 s56, s56, 1
	s_lshl_b32 s56, s56, 15
	s_add_i32 s44, s56, 0xfff68000
	s_add_i32 s56, s20, 7
	s_and_b32 s56, s56, 7
	s_lshl_b32 s56, s56, 1
	s_or_b32 s56, s56, 1
	s_lshl_b32 s56, s56, 15
	s_add_i32 s45, s56, 0xfff68000
	s_lshl_b32 s56, s20, 1
	s_lshl_b32 s56, s56, 15
	s_add_i32 s46, s56, 0xfffe8000
	s_lshl_b32 s56, s20, 1
	s_or_b32 s56, s56, 1
	s_lshl_b32 s56, s56, 15
	s_add_i32 s47, s56, 0xfffe8000
	s_add_i32 s56, s20, 1
	s_and_b32 s56, s56, 7
	s_lshl_b32 s56, s56, 1
	s_lshl_b32 s56, s56, 15
	s_add_i32 s48, s56, 0xfffe8000
	s_add_i32 s56, s20, 2
	s_and_b32 s56, s56, 7
	s_lshl_b32 s56, s56, 1
	s_lshl_b32 s56, s56, 15
	s_add_i32 s49, s56, 0xfffe8000
	s_lshl_b32 s56, s20, 1
	s_lshr_b32 s56, s56, 2
	s_lshl_b32 s64, s56, 8
	s_lshl_b32 s56, s20, 1
	s_or_b32 s56, s56, 1
	s_lshr_b32 s56, s56, 2
	s_lshl_b32 s65, s56, 8
	s_add_i32 s56, s20, 1
	s_and_b32 s56, s56, 7
	s_lshl_b32 s56, s56, 1
	s_lshr_b32 s56, s56, 2
	s_lshl_b32 s66, s56, 8
	s_add_i32 s56, s20, 2
	s_and_b32 s56, s56, 7
	s_lshl_b32 s56, s56, 1
	s_lshr_b32 s56, s56, 2
	s_lshl_b32 s67, s56, 8
	s_add_i32 s56, s20, 3
	s_and_b32 s56, s56, 7
	s_lshl_b32 s56, s56, 1
	s_lshr_b32 s56, s56, 2
	s_lshl_b32 s68, s56, 8
	s_add_i32 s56, s20, 4
	s_and_b32 s56, s56, 7
	s_lshl_b32 s56, s56, 1
	s_lshr_b32 s56, s56, 2
	s_lshl_b32 s69, s56, 8
	s_add_i32 s56, s20, 5
	s_and_b32 s56, s56, 7
	s_lshl_b32 s56, s56, 1
	s_lshr_b32 s56, s56, 2
	s_lshl_b32 s70, s56, 8
	s_add_i32 s56, s20, 6
	s_and_b32 s56, s56, 7
	s_lshl_b32 s56, s56, 1
	s_lshr_b32 s56, s56, 2
	s_lshl_b32 s71, s56, 8
	s_add_i32 s56, s20, 7
	s_and_b32 s56, s56, 7
	s_lshl_b32 s56, s56, 1
	s_lshr_b32 s56, s56, 2
	s_lshl_b32 s72, s56, 8
	s_add_i32 s56, s20, 1
	s_and_b32 s56, s56, 7
	s_lshl_b32 s56, s56, 1
	s_or_b32 s56, s56, 1
	s_lshr_b32 s56, s56, 2
	s_lshl_b32 s73, s56, 8
	s_add_i32 s56, s20, 2
	s_and_b32 s56, s56, 7
	s_lshl_b32 s56, s56, 1
	s_or_b32 s56, s56, 1
	s_lshr_b32 s56, s56, 2
	s_lshl_b32 s74, s56, 8
	s_add_i32 s56, s20, 3
	s_and_b32 s56, s56, 7
	s_lshl_b32 s56, s56, 1
	s_or_b32 s56, s56, 1
	s_lshr_b32 s56, s56, 2
	s_lshl_b32 s75, s56, 8
	s_add_i32 s56, s20, 4
	s_and_b32 s56, s56, 7
	s_lshl_b32 s56, s56, 1
	s_or_b32 s56, s56, 1
	s_lshr_b32 s56, s56, 2
	s_lshl_b32 s76, s56, 8
	s_add_i32 s56, s20, 5
	s_and_b32 s56, s56, 7
	s_lshl_b32 s56, s56, 1
	s_or_b32 s56, s56, 1
	s_lshr_b32 s56, s56, 2
	s_lshl_b32 s77, s56, 8
	s_add_i32 s56, s20, 6
	s_and_b32 s56, s56, 7
	s_lshl_b32 s56, s56, 1
	s_or_b32 s56, s56, 1
	s_lshr_b32 s56, s56, 2
	s_lshl_b32 s78, s56, 8
	s_add_i32 s56, s20, 7
	s_and_b32 s56, s56, 7
	s_lshl_b32 s56, s56, 1
	s_or_b32 s56, s56, 1
	s_lshr_b32 s56, s56, 2
	s_lshl_b32 s79, s56, 8
	s_and_b32 s56, s20, 1
	s_cmp_eq_u32 s56, 1
	s_cselect_b64 s[84:85], -1, 0
	buffer_load_dwordx4 v[58:61], v147, s[16:19], s60 offen
	buffer_load_dwordx4 v[54:57], v147, s[16:19], s60 offen offset:1024
	buffer_load_dwordx4 v[50:53], v147, s[16:19], s60 offen offset:2048
	buffer_load_dwordx4 v[38:41], v147, s[16:19], s60 offen offset:3072
	s_mov_b32 s10, 0xffff
	s_mov_b32 s0, 0x8000
	buffer_load_dwordx4 v[94:97], v147, s[16:19], s61 offen
	buffer_load_dwordx4 v[90:93], v147, s[16:19], s61 offen offset:1024
	buffer_load_dwordx4 v[78:81], v147, s[16:19], s61 offen offset:2048
	buffer_load_dwordx4 v[34:37], v147, s[16:19], s61 offen offset:3072
	s_mov_b32 s0, 0x10000
	buffer_load_dwordx4 v[82:85], v147, s[16:19], s62 offen
	buffer_load_dwordx4 v[70:73], v147, s[16:19], s62 offen offset:1024
	buffer_load_dwordx4 v[62:65], v147, s[16:19], s62 offen offset:2048
	buffer_load_dwordx4 v[42:45], v147, s[16:19], s62 offen offset:3072
	s_mov_b32 s0, 0x18000
	buffer_load_dwordx4 v[86:89], v147, s[16:19], s63 offen
	buffer_load_dwordx4 v[74:77], v147, s[16:19], s63 offen offset:1024
	buffer_load_dwordx4 v[66:69], v147, s[16:19], s63 offen offset:2048
	buffer_load_dwordx4 v[46:49], v147, s[16:19], s63 offen offset:3072
	s_waitcnt vmcnt(44)
	v_cvt_f16_f32_e32 v173, v174
	s_waitcnt vmcnt(43)
	v_cvt_f16_f32_e32 v175, v175
	v_lshlrev_b32_e32 v174, 1, v0
	v_or_b32_e32 v176, 0x12400, v174
	ds_write_b16 v176, v173
	v_or_b32_e32 v173, 0x12800, v174
	ds_write_b16 v173, v175
	v_add_u32_e32 v173, 0x12c00, v172
	s_mov_b32 s11, 1
	s_waitcnt vmcnt(39)
	ds_write_b128 v173, v[160:163]
	ds_write_b128 v173, v[148:151] offset:8192
	ds_write_b128 v173, v[152:155] offset:16384
	ds_write_b128 v173, v[156:159] offset:24576
	v_add_u32_e32 v148, 0x1ac00, v172
	s_cmpk_lt_u32 s22, 0x100
	s_waitcnt vmcnt(38)
	ds_write_b128 v148, v[164:167]
	s_waitcnt vmcnt(37)
	ds_write_b128 v148, v[168:171] offset:8192
	s_cbranch_scc1 .LBB1_2
	s_setprio 3
.LBB1_2:
	v_lshrrev_b32_e32 v151, 4, v137
	s_lshl_b64 s[6:7], s[2:3], 4
	v_cmp_eq_u32_e64 s[2:3], 1, v151
	s_waitcnt vmcnt(31)
	v_cvt_f16_f32_e32 v8, v8
	v_cmp_gt_u32_e32 vcc, 16, v137
	s_waitcnt vmcnt(29)
	v_cndmask_b32_e64 v116, 0, v116, s[2:3]
	s_waitcnt vmcnt(21)
	v_cndmask_b32_e64 v100, 0, v100, s[2:3]
	v_cmp_eq_u32_e64 s[0:1], 2, v151
	v_cndmask_b32_e64 v114, 0, v114, s[2:3]
	v_cndmask_b32_e64 v115, 0, v115, s[2:3]
	v_cndmask_b32_e32 v6, v116, v6, vcc
	v_cndmask_b32_e64 v116, 0, v117, s[2:3]
	v_cndmask_b32_e64 v108, 0, v108, s[2:3]
	v_cndmask_b32_e32 v26, v100, v26, vcc
	v_cvt_f16_f32_e32 v29, v29
	v_cndmask_b32_e64 v100, 0, v101, s[2:3]
	v_cndmask_b32_e32 v28, 0, v28, vcc
	v_cndmask_b32_e64 v152, 0, 1.0, s[0:1]
	v_cndmask_b32_e32 v114, v114, v120, vcc
	v_cndmask_b32_e32 v115, v115, v121, vcc
	v_cndmask_b32_e32 v7, v116, v7, vcc
	v_cndmask_b32_e64 v106, 0, v106, s[2:3]
	v_cndmask_b32_e64 v107, 0, v107, s[2:3]
	v_cndmask_b32_e32 v14, v108, v14, vcc
	v_cndmask_b32_e64 v108, 0, v109, s[2:3]
	v_cndmask_b32_e32 v27, v100, v27, vcc
	v_cvt_f16_f32_e32 v100, v28
	v_cndmask_b32_e32 v116, 0, v8, vcc
	v_cvt_pk_f16_f32 v8, v6, v7
	v_cvt_pk_f16_f32 v7, v114, v115
	v_cndmask_b32_e64 v114, v152, v140, s[2:3]
	v_cndmask_b32_e32 v106, v106, v112, vcc
	v_cndmask_b32_e32 v107, v107, v113, vcc
	v_cndmask_b32_e32 v15, v108, v15, vcc
	v_cndmask_b32_e64 v98, 0, v98, s[2:3]
	v_cndmask_b32_e64 v99, 0, v99, s[2:3]
	v_cndmask_b32_e32 v110, v114, v110, vcc
	v_cndmask_b32_e64 v114, 0, v141, s[2:3]
	v_cndmask_b32_e32 v108, 0, v16, vcc
	v_cvt_pk_f16_f32 v16, v14, v15
	v_cvt_pk_f16_f32 v15, v106, v107
	v_cndmask_b32_e64 v106, v152, v138, s[2:3]
	v_cndmask_b32_e32 v98, v98, v104, vcc
	v_cndmask_b32_e32 v99, v99, v105, vcc
	v_cndmask_b32_e32 v111, v114, v111, vcc
	v_cndmask_b32_e32 v102, v106, v102, vcc
	v_cndmask_b32_e64 v106, 0, v139, s[2:3]
	v_cndmask_b32_e32 v29, 0, v29, vcc
	v_cvt_pk_f16_f32 v28, v26, v27
	v_cvt_pk_f16_f32 v27, v98, v99
	v_lshlrev_b32_e32 v101, 10, v1
	v_bitop3_b32 v98, v151, v0, 3 bitop3:0x78
	v_lshl_add_u64 v[130:131], s[4:5], 0, v[130:131]
	v_cvt_f16_f32_e32 v4, v4
	v_cvt_pk_f16_f32 v14, v110, v111
	v_cndmask_b32_e32 v103, v106, v103, vcc
	v_pack_b32_f16 v29, v100, v29
	v_lshl_or_b32 v111, v98, 4, v101
	v_lshlrev_b32_e32 v100, 4, v1
	s_movk_i32 s4, 0xc0
	v_cndmask_b32_e64 v124, 0, v124, s[2:3]
	v_cvt_pk_f16_f32 v26, v102, v103
	v_and_b32_e32 v112, 0xc0, v100
	v_bitop3_b32 v100, v100, s4, v111 bitop3:0x26
	s_lshl_b32 s4, s20, 3
	v_lshrrev_b32_e32 v102, 5, v137
	v_lshrrev_b32_e32 v104, 1, v137
	v_cndmask_b32_e64 v122, 0, v122, s[2:3]
	v_cndmask_b32_e64 v123, 0, v123, s[2:3]
	v_cndmask_b32_e32 v2, v124, v2, vcc
	v_cvt_f16_f32_e32 v5, v5
	v_cndmask_b32_e64 v124, 0, v125, s[2:3]
	v_cvt_f16_f32_e32 v9, v9
	v_or_b32_e32 v103, s4, v102
	v_and_or_b32 v110, v104, 8, v101
	v_bitop3_b32 v101, s4, v1, v102 bitop3:0x36
	s_lshl_b32 s4, s20, 4
	v_cndmask_b32_e32 v122, v122, v128, vcc
	v_cndmask_b32_e32 v123, v123, v129, vcc
	v_cndmask_b32_e32 v3, v124, v3, vcc
	v_cndmask_b32_e32 v17, 0, v17, vcc
	v_lshlrev_b32_e32 v107, 4, v101
	v_bitop3_b32 v101, v103, v1, 2 bitop3:0x36
	s_add_i32 s4, s4, 0x10000
	v_bfe_u32 v0, v0, 4, 2
	v_cndmask_b32_e64 v144, v152, v144, s[2:3]
	v_cndmask_b32_e32 v124, 0, v4, vcc
	v_cvt_pk_f16_f32 v4, v2, v3
	v_cvt_pk_f16_f32 v3, v122, v123
	v_cndmask_b32_e64 v122, v152, v142, s[2:3]
	v_cvt_pk_f16_f32 v17, v108, v17
	s_movk_i32 s5, 0x80
	v_lshlrev_b32_e32 v108, 4, v101
	v_bitop3_b32 v101, v103, v1, 4 bitop3:0x36
	s_cmp_lt_u32 s22, 64
	v_lshlrev_b32_e32 v104, 5, v0
	v_lshlrev_b32_e32 v0, 6, v0
	v_cndmask_b32_e32 v126, v144, v126, vcc
	v_cndmask_b32_e64 v144, 0, v145, s[2:3]
	v_cndmask_b32_e32 v118, v122, v118, vcc
	v_cndmask_b32_e64 v122, 0, v143, s[2:3]
	v_bitop3_b32 v99, v112, s5, v111 bitop3:0x36
	v_lshlrev_b32_e32 v109, 4, v101
	v_bitop3_b32 v101, v103, v1, 6 bitop3:0x36
	v_lshl_or_b32 v105, s20, 8, v0
	v_mov_b32_e32 v0, 0x1ec00
	s_cselect_b64 s[4:5], -1, 0
	v_cndmask_b32_e32 v127, v144, v127, vcc
	v_cndmask_b32_e32 v5, 0, v5, vcc
	v_cndmask_b32_e32 v119, v122, v119, vcc
	v_cndmask_b32_e32 v9, 0, v9, vcc
	v_lshlrev_b32_e32 v113, 4, v101
	v_lshlrev_b32_e32 v101, 5, v1
	v_lshl_add_u32 v106, v137, 6, v0
	s_cmp_eq_u32 s20, 0
	s_cselect_b32 s31, 0, 0xffff1d00
	v_add_u32_e32 v106, s31, v106
	v_cndmask_b32_e64 v0, 0, 1, s[4:5]
	v_lshl_add_u64 v[132:133], s[8:9], 0, v[132:133]
	v_or_b32_e32 v148, 0x400, v147
	v_or_b32_e32 v149, 0x800, v147
	v_or_b32_e32 v150, 0xc00, v147
	v_cvt_pk_f16_f32 v2, v126, v127
	v_pack_b32_f16 v5, v124, v5
	v_cvt_pk_f16_f32 v6, v118, v119
	v_pack_b32_f16 v9, v116, v9
	v_bitop3_b32 v98, v112, 64, v111 bitop3:0x36
	v_lshl_or_b32 v104, s20, 7, v104
	s_mov_b32 s22, 0x98000
	s_mov_b32 s23, 0x5040100
	s_mov_b32 s24, 0x7060302
	v_add_u32_e32 v107, v107, v110
	v_add_u32_e32 v108, v108, v110
	v_add_u32_e32 v109, v109, v110
	v_add_u32_e32 v110, v113, v110
	v_add_u32_e32 v111, v112, v111
	v_lshlrev_b32_e32 v113, 4, v137
	v_or_b32_e32 v113, 0x10000, v113
	s_lshr_b32 s28, s20, 2
	s_and_b32 s29, s20, 3
	s_lshl_b32 s28, s28, 10
	s_lshl_b32 s29, s29, 2
	s_add_i32 s28, s28, s29
	v_add_u32_e32 v112, s28, v113
	v_cmp_eq_u32_e64 s[26:27], 3, v151
	v_add_u32_e32 v114, 0x12400, v101
	v_mov_b32_e32 v121, v111
	v_mov_b32_e32 v144, v98
	v_cndmask_b32_e64 v111, v111, v99, s[84:85]
	v_cndmask_b32_e64 v99, v99, v121, s[84:85]
	v_cndmask_b32_e64 v98, v98, v100, s[84:85]
	v_cndmask_b32_e64 v100, v100, v144, s[84:85]
	v_and_b32_e32 v108, 15, v137
	s_lshl_b32 s31, s20, 3
	v_add_u32_e32 v107, s31, v151
	v_xor_b32_e32 v107, v107, v108
	v_lshlrev_b32_e32 v107, 4, v107
	v_lshl_or_b32 v107, v108, 10, v107
	v_xor_b32_e32 v108, 64, v107
	v_cmp_ne_u32_e64 s[4:5], 1, v0
	s_waitcnt vmcnt(16)
	v_cndmask_b32_e64 v1, v30, v134, s[0:1]
	v_bfi_b32 v30, s10, v1, v30
	v_perm_b32 v1, v22, v134, s24
	v_cndmask_b32_e64 v22, v22, v1, s[0:1]
	v_bfi_b32 v1, s10, v135, v18
	v_perm_b32 v121, v10, v135, s24
	v_cndmask_b32_e64 v18, v18, v1, s[0:1]
	v_cndmask_b32_e64 v10, v10, v121, s[0:1]
	v_mov_b32_e32 v121, v136
	v_mov_b32_e32 v144, v136
	v_mov_b32_e32 v145, v136
	v_mov_b32_e32 v0, v136
	v_mov_b32_e32 v1, v136
	s_waitcnt lgkmcnt(0)
	s_barrier
	ds_read_u16 v102, v114
	ds_read_u16 v103, v114 offset:512
	ds_read_u16 v115, v114 offset:1024
	ds_read_u16 v116, v114 offset:1536
	v_add_u32_e32 v0, 0x12c00, v105
	ds_read_b128 v[240:243], v0
	ds_read_b128 v[244:247], v0 offset:16
	ds_read_b128 v[248:251], v0 offset:32
	ds_read_b128 v[252:255], v0 offset:48
	v_add_u32_e32 v114, 2, v114
	s_waitcnt lgkmcnt(0)
	s_branch .LBB1_4
.LBB1_4:
	s_and_saveexec_b64 s[32:33], s[2:3]
	v_perm_b32 v5, v1, v102, s23
	v_perm_b32 v9, v121, v103, s23
	s_or_b64 exec, exec, s[32:33]
	v_mov_b32_e32 v144, v1
	v_mov_b32_e32 v145, v121
	v_mfma_f32_16x16x32_f16 v[164:167], v[30:33], v[2:5], 0
	v_mfma_f32_16x16x32_f16 v[180:183], v[22:25], v[2:5], 0
	s_cmp_lg_u32 s22, 0x818000
	v_permlane32_swap_b32_e32 v1, v144
	v_permlane32_swap_b32_e32 v121, v145
	v_mfma_f32_16x16x32_f16 v[168:171], v[30:33], v[6:9], 0
	v_mfma_f32_16x16x32_f16 v[184:187], v[22:25], v[6:9], 0
	s_cselect_b32 s9, s11, 15
	s_and_saveexec_b64 s[32:33], s[2:3]
	v_perm_b32 v17, v144, v115, s23
	v_perm_b32 v29, v145, v116, s23
	s_or_b64 exec, exec, s[32:33]
	v_mfma_f32_16x16x32_f16 v[172:175], v[30:33], v[14:17], 0
	v_mfma_f32_16x16x32_f16 v[188:191], v[22:25], v[14:17], 0
	v_mfma_f32_16x16x32_f16 v[176:179], v[30:33], v[26:29], 0
	v_mfma_f32_16x16x32_f16 v[192:195], v[22:25], v[26:29], 0
	v_mfma_f32_16x16x32_f16 v[208:211], v[18:21], v[2:5], 0
	v_mfma_f32_16x16x32_f16 v[224:227], v[10:13], v[2:5], 0
	v_cvt_pk_f16_f32 v122, v164, v165
	v_cvt_pk_f16_f32 v123, v166, v167
	v_pk_max_f16 v122, v122, 0
	v_pk_max_f16 v123, v123, 0
	v_cvt_pk_f16_f32 v124, v180, v181
	v_cvt_pk_f16_f32 v125, v182, v183
	v_pk_max_f16 v124, v124, 0
	v_pk_max_f16 v125, v125, 0
	ds_write_b128 v107, v[122:125]
	v_mfma_f32_16x16x32_f16 v[212:215], v[18:21], v[6:9], 0
	v_mfma_f32_16x16x32_f16 v[228:231], v[10:13], v[6:9], 0
	v_cvt_pk_f16_f32 v126, v168, v169
	v_cvt_pk_f16_f32 v127, v170, v171
	v_pk_max_f16 v126, v126, 0
	v_pk_max_f16 v127, v127, 0
	v_cvt_pk_f16_f32 v128, v184, v185
	v_cvt_pk_f16_f32 v129, v186, v187
	v_pk_max_f16 v128, v128, 0
	v_pk_max_f16 v129, v129, 0
	ds_write_b128 v107, v[126:129] offset:16384
	v_mfma_f32_16x16x32_f16 v[216:219], v[18:21], v[14:17], 0
	v_mfma_f32_16x16x32_f16 v[232:235], v[10:13], v[14:17], 0
	v_cvt_pk_f16_f32 v134, v172, v173
	v_cvt_pk_f16_f32 v135, v174, v175
	v_pk_max_f16 v134, v134, 0
	v_pk_max_f16 v135, v135, 0
	v_cvt_pk_f16_f32 v136, v188, v189
	v_cvt_pk_f16_f32 v137, v190, v191
	v_pk_max_f16 v136, v136, 0
	v_pk_max_f16 v137, v137, 0
	ds_write_b128 v107, v[134:137] offset:32768
	v_mfma_f32_16x16x32_f16 v[220:223], v[18:21], v[26:29], 0
	v_mfma_f32_16x16x32_f16 v[236:239], v[10:13], v[26:29], 0
	v_cvt_pk_f16_f32 v138, v176, v177
	v_cvt_pk_f16_f32 v139, v178, v179
	v_pk_max_f16 v138, v138, 0
	v_pk_max_f16 v139, v139, 0
	v_cvt_pk_f16_f32 v140, v192, v193
	v_cvt_pk_f16_f32 v141, v194, v195
	v_pk_max_f16 v140, v140, 0
	v_pk_max_f16 v141, v141, 0
	ds_write_b128 v107, v[138:141] offset:49152
	s_lshl_b32 s20, s9, 7
	v_lshl_add_u64 v[0:1], s[20:21], 3, v[132:133]
	s_add_i32 s25, s22, s34
	s_lshl_b32 s8, s9, 8
	buffer_load_dwordx4 v[192:195], v147, s[16:19], s25 offen
	buffer_load_dwordx4 v[196:199], v148, s[16:19], s25 offen
	buffer_load_dwordx4 v[200:203], v149, s[16:19], s25 offen
	buffer_load_dwordx4 v[204:207], v150, s[16:19], s25 offen
	s_waitcnt vmcnt(19)
	v_mfma_f32_16x16x32_f16 v[164:167], v[58:61], v[122:125], v[240:243]
	v_cvt_pk_f16_f32 v142, v208, v209
	v_cvt_pk_f16_f32 v143, v210, v211
	v_mfma_f32_16x16x32_f16 v[168:171], v[58:61], v[126:129], v[240:243]
	v_pk_max_f16 v142, v142, 0
	v_pk_max_f16 v143, v143, 0
	v_mfma_f32_16x16x32_f16 v[172:175], v[58:61], v[134:137], v[240:243]
	v_cvt_pk_f16_f32 v144, v224, v225
	v_cvt_pk_f16_f32 v145, v226, v227
	v_mfma_f32_16x16x32_f16 v[10:13], v[58:61], v[138:141], v[240:243]
	v_pk_max_f16 v144, v144, 0
	v_pk_max_f16 v145, v145, 0
	ds_write_b128 v108, v[142:145]
	s_waitcnt vmcnt(18)
	v_mfma_f32_16x16x32_f16 v[58:61], v[54:57], v[122:125], v[244:247]
	v_cvt_pk_f16_f32 v152, v212, v213
	v_cvt_pk_f16_f32 v153, v214, v215
	v_mfma_f32_16x16x32_f16 v[176:179], v[54:57], v[126:129], v[244:247]
	v_pk_max_f16 v152, v152, 0
	v_pk_max_f16 v153, v153, 0
	v_mfma_f32_16x16x32_f16 v[180:183], v[54:57], v[134:137], v[244:247]
	v_cvt_pk_f16_f32 v154, v228, v229
	v_cvt_pk_f16_f32 v155, v230, v231
	v_mfma_f32_16x16x32_f16 v[18:21], v[54:57], v[138:141], v[244:247]
	v_pk_max_f16 v154, v154, 0
	v_pk_max_f16 v155, v155, 0
	ds_write_b128 v108, v[152:155] offset:16384
	s_waitcnt vmcnt(17)
	v_mfma_f32_16x16x32_f16 v[54:57], v[50:53], v[122:125], v[248:251]
	v_cvt_pk_f16_f32 v156, v216, v217
	v_cvt_pk_f16_f32 v157, v218, v219
	v_mfma_f32_16x16x32_f16 v[184:187], v[50:53], v[126:129], v[248:251]
	v_pk_max_f16 v156, v156, 0
	v_pk_max_f16 v157, v157, 0
	v_mfma_f32_16x16x32_f16 v[188:191], v[50:53], v[134:137], v[248:251]
	v_cvt_pk_f16_f32 v158, v232, v233
	v_cvt_pk_f16_f32 v159, v234, v235
	v_mfma_f32_16x16x32_f16 v[22:25], v[50:53], v[138:141], v[248:251]
	v_pk_max_f16 v158, v158, 0
	v_pk_max_f16 v159, v159, 0
	ds_write_b128 v108, v[156:159] offset:32768
	s_waitcnt vmcnt(16)
	v_mfma_f32_16x16x32_f16 v[50:53], v[38:41], v[122:125], v[252:255]
	v_cvt_pk_f16_f32 v160, v220, v221
	v_cvt_pk_f16_f32 v161, v222, v223
	v_mfma_f32_16x16x32_f16 v[122:125], v[38:41], v[126:129], v[252:255]
	v_pk_max_f16 v160, v160, 0
	v_pk_max_f16 v161, v161, 0
	v_mfma_f32_16x16x32_f16 v[126:129], v[38:41], v[134:137], v[252:255]
	v_cvt_pk_f16_f32 v162, v236, v237
	v_cvt_pk_f16_f32 v163, v238, v239
	v_mfma_f32_16x16x32_f16 v[38:41], v[38:41], v[138:141], v[252:255]
	v_pk_max_f16 v162, v162, 0
	v_pk_max_f16 v163, v163, 0
	ds_write_b128 v108, v[160:163] offset:49152
	s_add_i32 s9, s22, s35
	s_waitcnt vmcnt(15)
	v_mfma_f32_16x16x32_f16 v[164:167], v[94:97], v[142:145], v[164:167]
	v_mfma_f32_16x16x32_f16 v[168:171], v[94:97], v[152:155], v[168:171]
	s_waitcnt vmcnt(14)
	v_mfma_f32_16x16x32_f16 v[58:61], v[90:93], v[142:145], v[58:61]
	v_mfma_f32_16x16x32_f16 v[176:179], v[90:93], v[152:155], v[176:179]
	s_waitcnt vmcnt(13)
	v_mfma_f32_16x16x32_f16 v[54:57], v[78:81], v[142:145], v[54:57]
	v_mfma_f32_16x16x32_f16 v[184:187], v[78:81], v[152:155], v[184:187]
	s_waitcnt vmcnt(12)
	v_mfma_f32_16x16x32_f16 v[50:53], v[34:37], v[142:145], v[50:53]
	buffer_load_dwordx4 v[140:143], v147, s[16:19], s9 offen
	buffer_load_dwordx4 v[220:223], v148, s[16:19], s9 offen
	v_mfma_f32_16x16x32_f16 v[122:125], v[34:37], v[152:155], v[122:125]
	buffer_load_dwordx4 v[152:155], v149, s[16:19], s9 offen
	buffer_load_dwordx4 v[224:227], v150, s[16:19], s9 offen
	s_mov_b32 s9, s21
	s_waitcnt lgkmcnt(4)
	s_barrier
	v_add_u32_e32 v117, s66, v99
	ds_read_b128 v[136:139], v117
	ds_read_b128 v[208:211], v117 offset:16384
	ds_read_b128 v[212:215], v117 offset:32768
	ds_read_b128 v[216:219], v117 offset:49152
	v_mfma_f32_16x16x32_f16 v[172:175], v[94:97], v[156:159], v[172:175]
	v_mfma_f32_16x16x32_f16 v[94:97], v[94:97], v[160:163], v[10:13]
	s_nop 2
	v_lshl_add_u64 v[10:11], s[8:9], 4, v[130:131]
	v_mfma_f32_16x16x32_f16 v[180:183], v[90:93], v[156:159], v[180:183]
	v_mfma_f32_16x16x32_f16 v[90:93], v[90:93], v[160:163], v[18:21]
	v_mfma_f32_16x16x32_f16 v[188:191], v[78:81], v[156:159], v[188:191]
	v_mfma_f32_16x16x32_f16 v[78:81], v[78:81], v[160:163], v[22:25]
	global_load_dwordx4 v[30:33], v[10:11], off
	s_nop 1
	global_load_dwordx4 v[22:25], v[10:11], off offset:1024
	global_load_dwordx4 v[18:21], v[10:11], off offset:2048
	s_nop 0
	global_load_dwordx4 v[10:13], v[10:11], off offset:3072
	s_nop 0
	global_load_dwordx2 v[134:135], v[0:1], off
	v_mfma_f32_16x16x32_f16 v[126:129], v[34:37], v[156:159], v[126:129]
	v_mfma_f32_16x16x32_f16 v[34:37], v[34:37], v[160:163], v[38:41]
	s_nop 2
	v_add_u32_e32 v117, s67, v111
	ds_read_b128 v[38:41], v117
	ds_read_b128 v[156:159], v117 offset:16384
	ds_read_b128 v[160:163], v117 offset:32768
	ds_read_b128 v[228:231], v117 offset:49152
	s_add_i32 s8, s22, s36
	s_waitcnt vmcnt(20) lgkmcnt(7)
	v_mfma_f32_16x16x32_f16 v[164:167], v[82:85], v[136:139], v[164:167]
	s_waitcnt lgkmcnt(6)
	v_mfma_f32_16x16x32_f16 v[168:171], v[82:85], v[208:211], v[168:171]
	s_waitcnt lgkmcnt(5)
	v_mfma_f32_16x16x32_f16 v[172:175], v[82:85], v[212:215], v[172:175]
	s_waitcnt lgkmcnt(4)
	v_mfma_f32_16x16x32_f16 v[82:85], v[82:85], v[216:219], v[94:97]
	s_waitcnt vmcnt(19)
	v_mfma_f32_16x16x32_f16 v[58:61], v[70:73], v[136:139], v[58:61]
	v_mfma_f32_16x16x32_f16 v[94:97], v[70:73], v[208:211], v[176:179]
	v_mfma_f32_16x16x32_f16 v[176:179], v[70:73], v[212:215], v[180:183]
	v_mfma_f32_16x16x32_f16 v[70:73], v[70:73], v[216:219], v[90:93]
	s_waitcnt vmcnt(18)
	v_mfma_f32_16x16x32_f16 v[54:57], v[62:65], v[136:139], v[54:57]
	v_mfma_f32_16x16x32_f16 v[90:93], v[62:65], v[208:211], v[184:187]
	v_mfma_f32_16x16x32_f16 v[180:183], v[62:65], v[212:215], v[188:191]
	v_mfma_f32_16x16x32_f16 v[62:65], v[62:65], v[216:219], v[78:81]
	s_waitcnt vmcnt(17)
	v_mfma_f32_16x16x32_f16 v[50:53], v[42:45], v[136:139], v[50:53]
	v_mfma_f32_16x16x32_f16 v[78:81], v[42:45], v[208:211], v[122:125]
	v_mfma_f32_16x16x32_f16 v[122:125], v[42:45], v[212:215], v[126:129]
	s_nop 2
	buffer_load_dwordx4 v[126:129], v147, s[16:19], s8 offen
	buffer_load_dwordx4 v[136:139], v148, s[16:19], s8 offen
	buffer_load_dwordx4 v[184:187], v149, s[16:19], s8 offen
	buffer_load_dwordx4 v[188:191], v150, s[16:19], s8 offen
	v_mfma_f32_16x16x32_f16 v[34:37], v[42:45], v[216:219], v[34:37]
	v_add_u32_e32 v117, s68, v99
	ds_read_b128 v[42:45], v117
	ds_read_b128 v[208:211], v117 offset:16384
	ds_read_b128 v[212:215], v117 offset:32768
	ds_read_b128 v[216:219], v117 offset:49152
	s_add_i32 s8, s22, s37
	s_waitcnt vmcnt(20) lgkmcnt(7)
	v_mfma_f32_16x16x32_f16 v[164:167], v[86:89], v[38:41], v[164:167]
	s_waitcnt lgkmcnt(6)
	v_mfma_f32_16x16x32_f16 v[168:171], v[86:89], v[156:159], v[168:171]
	s_waitcnt lgkmcnt(5)
	v_mfma_f32_16x16x32_f16 v[172:175], v[86:89], v[160:163], v[172:175]
	s_waitcnt lgkmcnt(4)
	v_mfma_f32_16x16x32_f16 v[82:85], v[86:89], v[228:231], v[82:85]
	s_waitcnt vmcnt(19)
	v_mfma_f32_16x16x32_f16 v[58:61], v[74:77], v[38:41], v[58:61]
	v_mfma_f32_16x16x32_f16 v[86:89], v[74:77], v[156:159], v[94:97]
	v_mfma_f32_16x16x32_f16 v[94:97], v[74:77], v[160:163], v[176:179]
	v_mfma_f32_16x16x32_f16 v[70:73], v[74:77], v[228:231], v[70:73]
	s_waitcnt vmcnt(18)
	v_mfma_f32_16x16x32_f16 v[54:57], v[66:69], v[38:41], v[54:57]
	v_mfma_f32_16x16x32_f16 v[74:77], v[66:69], v[156:159], v[90:93]
	v_mfma_f32_16x16x32_f16 v[90:93], v[66:69], v[160:163], v[180:183]
	v_mfma_f32_16x16x32_f16 v[62:65], v[66:69], v[228:231], v[62:65]
	s_waitcnt vmcnt(17)
	v_mfma_f32_16x16x32_f16 v[38:41], v[46:49], v[38:41], v[50:53]
	v_mfma_f32_16x16x32_f16 v[50:53], v[46:49], v[156:159], v[78:81]
	v_mfma_f32_16x16x32_f16 v[66:69], v[46:49], v[160:163], v[122:125]
	s_nop 1
	buffer_load_dwordx4 v[78:81], v147, s[16:19], s8 offen
	buffer_load_dwordx4 v[122:125], v148, s[16:19], s8 offen
	buffer_load_dwordx4 v[156:159], v149, s[16:19], s8 offen
	buffer_load_dwordx4 v[160:163], v150, s[16:19], s8 offen
	v_mfma_f32_16x16x32_f16 v[34:37], v[46:49], v[228:231], v[34:37]
	v_add_u32_e32 v117, s69, v111
	ds_read_b128 v[46:49], v117
	ds_read_b128 v[176:179], v117 offset:16384
	ds_read_b128 v[180:183], v117 offset:32768
	ds_read_b128 v[228:231], v117 offset:49152
	s_add_i32 s8, s22, s38
	s_waitcnt vmcnt(20) lgkmcnt(7)
	v_mfma_f32_16x16x32_f16 v[164:167], v[192:195], v[42:45], v[164:167]
	s_waitcnt lgkmcnt(6)
	v_mfma_f32_16x16x32_f16 v[168:171], v[192:195], v[208:211], v[168:171]
	s_waitcnt lgkmcnt(5)
	v_mfma_f32_16x16x32_f16 v[172:175], v[192:195], v[212:215], v[172:175]
	s_waitcnt lgkmcnt(4)
	v_mfma_f32_16x16x32_f16 v[82:85], v[192:195], v[216:219], v[82:85]
	s_waitcnt vmcnt(19)
	v_mfma_f32_16x16x32_f16 v[58:61], v[196:199], v[42:45], v[58:61]
	v_mfma_f32_16x16x32_f16 v[86:89], v[196:199], v[208:211], v[86:89]
	v_mfma_f32_16x16x32_f16 v[94:97], v[196:199], v[212:215], v[94:97]
	v_mfma_f32_16x16x32_f16 v[70:73], v[196:199], v[216:219], v[70:73]
	s_waitcnt vmcnt(18)
	v_mfma_f32_16x16x32_f16 v[54:57], v[200:203], v[42:45], v[54:57]
	v_mfma_f32_16x16x32_f16 v[74:77], v[200:203], v[208:211], v[74:77]
	v_mfma_f32_16x16x32_f16 v[90:93], v[200:203], v[212:215], v[90:93]
	v_mfma_f32_16x16x32_f16 v[62:65], v[200:203], v[216:219], v[62:65]
	s_waitcnt vmcnt(17)
	v_mfma_f32_16x16x32_f16 v[38:41], v[204:207], v[42:45], v[38:41]
	v_mfma_f32_16x16x32_f16 v[42:45], v[204:207], v[208:211], v[50:53]
	v_mfma_f32_16x16x32_f16 v[50:53], v[204:207], v[212:215], v[66:69]
	s_nop 2
	buffer_load_dwordx4 v[66:69], v147, s[16:19], s8 offen
	buffer_load_dwordx4 v[192:195], v148, s[16:19], s8 offen
	buffer_load_dwordx4 v[196:199], v149, s[16:19], s8 offen
	buffer_load_dwordx4 v[200:203], v150, s[16:19], s8 offen
	v_mfma_f32_16x16x32_f16 v[34:37], v[204:207], v[216:219], v[34:37]
	v_add_u32_e32 v117, s70, v99
	ds_read_b128 v[204:207], v117
	ds_read_b128 v[208:211], v117 offset:16384
	ds_read_b128 v[212:215], v117 offset:32768
	ds_read_b128 v[216:219], v117 offset:49152
	s_add_i32 s8, s22, s39
	s_waitcnt vmcnt(20) lgkmcnt(7)
	v_mfma_f32_16x16x32_f16 v[164:167], v[140:143], v[46:49], v[164:167]
	s_waitcnt lgkmcnt(6)
	v_mfma_f32_16x16x32_f16 v[168:171], v[140:143], v[176:179], v[168:171]
	s_waitcnt lgkmcnt(5)
	v_mfma_f32_16x16x32_f16 v[172:175], v[140:143], v[180:183], v[172:175]
	s_waitcnt lgkmcnt(4)
	v_mfma_f32_16x16x32_f16 v[82:85], v[140:143], v[228:231], v[82:85]
	s_waitcnt vmcnt(19)
	v_mfma_f32_16x16x32_f16 v[58:61], v[220:223], v[46:49], v[58:61]
	v_mfma_f32_16x16x32_f16 v[86:89], v[220:223], v[176:179], v[86:89]
	s_waitcnt vmcnt(18)
	v_mfma_f32_16x16x32_f16 v[54:57], v[152:155], v[46:49], v[54:57]
	v_mfma_f32_16x16x32_f16 v[74:77], v[152:155], v[176:179], v[74:77]
	v_mfma_f32_16x16x32_f16 v[90:93], v[152:155], v[180:183], v[90:93]
	v_mfma_f32_16x16x32_f16 v[62:65], v[152:155], v[228:231], v[62:65]
	s_waitcnt vmcnt(17)
	v_mfma_f32_16x16x32_f16 v[38:41], v[224:227], v[46:49], v[38:41]
	v_mfma_f32_16x16x32_f16 v[42:45], v[224:227], v[176:179], v[42:45]
	v_mfma_f32_16x16x32_f16 v[46:49], v[224:227], v[180:183], v[50:53]
	s_nop 2
	buffer_load_dwordx4 v[50:53], v147, s[16:19], s8 offen
	buffer_load_dwordx4 v[140:143], v148, s[16:19], s8 offen
	buffer_load_dwordx4 v[152:155], v149, s[16:19], s8 offen
	buffer_load_dwordx4 v[176:179], v150, s[16:19], s8 offen
	v_mfma_f32_16x16x32_f16 v[94:97], v[220:223], v[180:183], v[94:97]
	v_mfma_f32_16x16x32_f16 v[70:73], v[220:223], v[228:231], v[70:73]
	v_mfma_f32_16x16x32_f16 v[34:37], v[224:227], v[228:231], v[34:37]
	v_add_u32_e32 v117, s71, v111
	ds_read_b128 v[180:183], v117
	ds_read_b128 v[220:223], v117 offset:16384
	ds_read_b128 v[224:227], v117 offset:32768
	ds_read_b128 v[228:231], v117 offset:49152
	s_add_i32 s8, s22, s40
	s_waitcnt vmcnt(15) lgkmcnt(7)
	v_mfma_f32_16x16x32_f16 v[164:167], v[126:129], v[204:207], v[164:167]
	s_waitcnt lgkmcnt(6)
	v_mfma_f32_16x16x32_f16 v[168:171], v[126:129], v[208:211], v[168:171]
	s_waitcnt lgkmcnt(5)
	v_mfma_f32_16x16x32_f16 v[172:175], v[126:129], v[212:215], v[172:175]
	s_waitcnt lgkmcnt(4)
	v_mfma_f32_16x16x32_f16 v[82:85], v[126:129], v[216:219], v[82:85]
	s_waitcnt vmcnt(14)
	v_mfma_f32_16x16x32_f16 v[58:61], v[136:139], v[204:207], v[58:61]
	v_mfma_f32_16x16x32_f16 v[86:89], v[136:139], v[208:211], v[86:89]
	v_mfma_f32_16x16x32_f16 v[94:97], v[136:139], v[212:215], v[94:97]
	v_mfma_f32_16x16x32_f16 v[70:73], v[136:139], v[216:219], v[70:73]
	s_waitcnt vmcnt(13)
	v_mfma_f32_16x16x32_f16 v[54:57], v[184:187], v[204:207], v[54:57]
	v_mfma_f32_16x16x32_f16 v[74:77], v[184:187], v[208:211], v[74:77]
	v_mfma_f32_16x16x32_f16 v[90:93], v[184:187], v[212:215], v[90:93]
	v_mfma_f32_16x16x32_f16 v[62:65], v[184:187], v[216:219], v[62:65]
	s_waitcnt vmcnt(12)
	v_mfma_f32_16x16x32_f16 v[38:41], v[188:191], v[204:207], v[38:41]
	buffer_load_dwordx4 v[126:129], v147, s[16:19], s8 offen
	buffer_load_dwordx4 v[136:139], v148, s[16:19], s8 offen
	buffer_load_dwordx4 v[184:187], v149, s[16:19], s8 offen
	buffer_load_dwordx4 v[204:207], v150, s[16:19], s8 offen
	v_mfma_f32_16x16x32_f16 v[42:45], v[188:191], v[208:211], v[42:45]
	v_mfma_f32_16x16x32_f16 v[46:49], v[188:191], v[212:215], v[46:49]
	v_mfma_f32_16x16x32_f16 v[34:37], v[188:191], v[216:219], v[34:37]
	v_add_u32_e32 v117, s72, v99
	ds_read_b128 v[188:191], v117
	ds_read_b128 v[208:211], v117 offset:16384
	ds_read_b128 v[212:215], v117 offset:32768
	ds_read_b128 v[216:219], v117 offset:49152
	s_add_i32 s8, s22, s41
	s_waitcnt vmcnt(15) lgkmcnt(7)
	v_mfma_f32_16x16x32_f16 v[164:167], v[78:81], v[180:183], v[164:167]
	s_waitcnt lgkmcnt(6)
	v_mfma_f32_16x16x32_f16 v[168:171], v[78:81], v[220:223], v[168:171]
	s_waitcnt lgkmcnt(5)
	v_mfma_f32_16x16x32_f16 v[172:175], v[78:81], v[224:227], v[172:175]
	s_waitcnt lgkmcnt(4)
	v_mfma_f32_16x16x32_f16 v[78:81], v[78:81], v[228:231], v[82:85]
	s_waitcnt vmcnt(14)
	v_mfma_f32_16x16x32_f16 v[58:61], v[122:125], v[180:183], v[58:61]
	v_mfma_f32_16x16x32_f16 v[82:85], v[122:125], v[220:223], v[86:89]
	v_mfma_f32_16x16x32_f16 v[86:89], v[122:125], v[224:227], v[94:97]
	v_mfma_f32_16x16x32_f16 v[70:73], v[122:125], v[228:231], v[70:73]
	s_waitcnt vmcnt(13)
	v_mfma_f32_16x16x32_f16 v[54:57], v[156:159], v[180:183], v[54:57]
	v_mfma_f32_16x16x32_f16 v[74:77], v[156:159], v[220:223], v[74:77]
	v_mfma_f32_16x16x32_f16 v[90:93], v[156:159], v[224:227], v[90:93]
	v_mfma_f32_16x16x32_f16 v[62:65], v[156:159], v[228:231], v[62:65]
	s_waitcnt vmcnt(12)
	v_mfma_f32_16x16x32_f16 v[38:41], v[160:163], v[180:183], v[38:41]
	buffer_load_dwordx4 v[94:97], v147, s[16:19], s8 offen
	buffer_load_dwordx4 v[122:125], v148, s[16:19], s8 offen
	buffer_load_dwordx4 v[156:159], v149, s[16:19], s8 offen
	buffer_load_dwordx4 v[180:183], v150, s[16:19], s8 offen
	v_mfma_f32_16x16x32_f16 v[42:45], v[160:163], v[220:223], v[42:45]
	v_mfma_f32_16x16x32_f16 v[46:49], v[160:163], v[224:227], v[46:49]
	v_mfma_f32_16x16x32_f16 v[34:37], v[160:163], v[228:231], v[34:37]
	s_waitcnt lgkmcnt(4)
	s_barrier
	v_add_u32_e32 v117, s73, v100
	ds_read_b128 v[160:163], v117
	ds_read_b128 v[220:223], v117 offset:16384
	ds_read_b128 v[224:227], v117 offset:32768
	ds_read_b128 v[228:231], v117 offset:49152
	s_add_i32 s8, s22, s42
	s_waitcnt vmcnt(15) lgkmcnt(7)
	v_mfma_f32_16x16x32_f16 v[164:167], v[66:69], v[188:191], v[164:167]
	s_waitcnt lgkmcnt(6)
	v_mfma_f32_16x16x32_f16 v[168:171], v[66:69], v[208:211], v[168:171]
	s_waitcnt lgkmcnt(5)
	v_mfma_f32_16x16x32_f16 v[172:175], v[66:69], v[212:215], v[172:175]
	s_waitcnt lgkmcnt(4)
	v_mfma_f32_16x16x32_f16 v[66:69], v[66:69], v[216:219], v[78:81]
	s_waitcnt vmcnt(14)
	v_mfma_f32_16x16x32_f16 v[58:61], v[192:195], v[188:191], v[58:61]
	v_mfma_f32_16x16x32_f16 v[78:81], v[192:195], v[208:211], v[82:85]
	v_mfma_f32_16x16x32_f16 v[82:85], v[192:195], v[212:215], v[86:89]
	v_mfma_f32_16x16x32_f16 v[70:73], v[192:195], v[216:219], v[70:73]
	s_waitcnt vmcnt(13)
	v_mfma_f32_16x16x32_f16 v[54:57], v[196:199], v[188:191], v[54:57]
	v_mfma_f32_16x16x32_f16 v[74:77], v[196:199], v[208:211], v[74:77]
	v_mfma_f32_16x16x32_f16 v[86:89], v[196:199], v[212:215], v[90:93]
	v_mfma_f32_16x16x32_f16 v[62:65], v[196:199], v[216:219], v[62:65]
	s_waitcnt vmcnt(12)
	v_mfma_f32_16x16x32_f16 v[38:41], v[200:203], v[188:191], v[38:41]
	buffer_load_dwordx4 v[90:93], v147, s[16:19], s8 offen
	buffer_load_dwordx4 v[188:191], v148, s[16:19], s8 offen
	buffer_load_dwordx4 v[192:195], v149, s[16:19], s8 offen
	buffer_load_dwordx4 v[196:199], v150, s[16:19], s8 offen
	v_mfma_f32_16x16x32_f16 v[42:45], v[200:203], v[208:211], v[42:45]
	v_mfma_f32_16x16x32_f16 v[46:49], v[200:203], v[212:215], v[46:49]
	v_mfma_f32_16x16x32_f16 v[34:37], v[200:203], v[216:219], v[34:37]
	v_add_u32_e32 v117, s74, v98
	ds_read_b128 v[200:203], v117
	ds_read_b128 v[208:211], v117 offset:16384
	ds_read_b128 v[212:215], v117 offset:32768
	ds_read_b128 v[216:219], v117 offset:49152
	s_add_i32 s8, s22, s43
	s_waitcnt vmcnt(15) lgkmcnt(7)
	v_mfma_f32_16x16x32_f16 v[164:167], v[50:53], v[160:163], v[164:167]
	s_waitcnt lgkmcnt(6)
	v_mfma_f32_16x16x32_f16 v[168:171], v[50:53], v[220:223], v[168:171]
	s_waitcnt lgkmcnt(5)
	v_mfma_f32_16x16x32_f16 v[172:175], v[50:53], v[224:227], v[172:175]
	s_waitcnt lgkmcnt(4)
	v_mfma_f32_16x16x32_f16 v[50:53], v[50:53], v[228:231], v[66:69]
	s_waitcnt vmcnt(14)
	v_mfma_f32_16x16x32_f16 v[58:61], v[140:143], v[160:163], v[58:61]
	v_mfma_f32_16x16x32_f16 v[66:69], v[140:143], v[220:223], v[78:81]
	v_mfma_f32_16x16x32_f16 v[78:81], v[140:143], v[224:227], v[82:85]
	v_mfma_f32_16x16x32_f16 v[70:73], v[140:143], v[228:231], v[70:73]
	s_waitcnt vmcnt(13)
	v_mfma_f32_16x16x32_f16 v[54:57], v[152:155], v[160:163], v[54:57]
	v_mfma_f32_16x16x32_f16 v[74:77], v[152:155], v[220:223], v[74:77]
	v_mfma_f32_16x16x32_f16 v[82:85], v[152:155], v[224:227], v[86:89]
	v_mfma_f32_16x16x32_f16 v[62:65], v[152:155], v[228:231], v[62:65]
	s_waitcnt vmcnt(12)
	v_mfma_f32_16x16x32_f16 v[38:41], v[176:179], v[160:163], v[38:41]
	buffer_load_dwordx4 v[86:89], v147, s[16:19], s8 offen
	buffer_load_dwordx4 v[140:143], v148, s[16:19], s8 offen
	buffer_load_dwordx4 v[152:155], v149, s[16:19], s8 offen
	buffer_load_dwordx4 v[160:163], v150, s[16:19], s8 offen
	v_mfma_f32_16x16x32_f16 v[42:45], v[176:179], v[220:223], v[42:45]
	v_mfma_f32_16x16x32_f16 v[46:49], v[176:179], v[224:227], v[46:49]
	v_mfma_f32_16x16x32_f16 v[34:37], v[176:179], v[228:231], v[34:37]
	v_add_u32_e32 v117, s75, v100
	ds_read_b128 v[176:179], v117
	ds_read_b128 v[220:223], v117 offset:16384
	ds_read_b128 v[224:227], v117 offset:32768
	ds_read_b128 v[228:231], v117 offset:49152
	s_add_i32 s8, s22, s44
	s_waitcnt vmcnt(15) lgkmcnt(7)
	v_mfma_f32_16x16x32_f16 v[164:167], v[126:129], v[200:203], v[164:167]
	s_waitcnt lgkmcnt(6)
	v_mfma_f32_16x16x32_f16 v[168:171], v[126:129], v[208:211], v[168:171]
	s_waitcnt lgkmcnt(5)
	v_mfma_f32_16x16x32_f16 v[172:175], v[126:129], v[212:215], v[172:175]
	s_waitcnt lgkmcnt(4)
	v_mfma_f32_16x16x32_f16 v[50:53], v[126:129], v[216:219], v[50:53]
	s_waitcnt vmcnt(14)
	v_mfma_f32_16x16x32_f16 v[58:61], v[136:139], v[200:203], v[58:61]
	v_mfma_f32_16x16x32_f16 v[66:69], v[136:139], v[208:211], v[66:69]
	v_mfma_f32_16x16x32_f16 v[78:81], v[136:139], v[212:215], v[78:81]
	v_mfma_f32_16x16x32_f16 v[70:73], v[136:139], v[216:219], v[70:73]
	s_waitcnt vmcnt(13)
	v_mfma_f32_16x16x32_f16 v[54:57], v[184:187], v[200:203], v[54:57]
	v_mfma_f32_16x16x32_f16 v[74:77], v[184:187], v[208:211], v[74:77]
	v_mfma_f32_16x16x32_f16 v[82:85], v[184:187], v[212:215], v[82:85]
	v_mfma_f32_16x16x32_f16 v[62:65], v[184:187], v[216:219], v[62:65]
	s_waitcnt vmcnt(12)
	v_mfma_f32_16x16x32_f16 v[38:41], v[204:207], v[200:203], v[38:41]
	buffer_load_dwordx4 v[126:129], v147, s[16:19], s8 offen
	buffer_load_dwordx4 v[136:139], v148, s[16:19], s8 offen
	buffer_load_dwordx4 v[184:187], v149, s[16:19], s8 offen
	buffer_load_dwordx4 v[200:203], v150, s[16:19], s8 offen
	v_mfma_f32_16x16x32_f16 v[42:45], v[204:207], v[208:211], v[42:45]
	v_mfma_f32_16x16x32_f16 v[46:49], v[204:207], v[212:215], v[46:49]
	v_mfma_f32_16x16x32_f16 v[34:37], v[204:207], v[216:219], v[34:37]
	v_add_u32_e32 v117, s76, v98
	ds_read_b128 v[204:207], v117
	ds_read_b128 v[208:211], v117 offset:16384
	ds_read_b128 v[212:215], v117 offset:32768
	ds_read_b128 v[216:219], v117 offset:49152
	s_add_i32 s8, s22, s45
	s_waitcnt vmcnt(15) lgkmcnt(7)
	v_mfma_f32_16x16x32_f16 v[164:167], v[94:97], v[176:179], v[164:167]
	s_waitcnt lgkmcnt(6)
	v_mfma_f32_16x16x32_f16 v[168:171], v[94:97], v[220:223], v[168:171]
	s_waitcnt vmcnt(14)
	v_mfma_f32_16x16x32_f16 v[58:61], v[122:125], v[176:179], v[58:61]
	v_mfma_f32_16x16x32_f16 v[66:69], v[122:125], v[220:223], v[66:69]
	s_waitcnt lgkmcnt(5)
	v_mfma_f32_16x16x32_f16 v[78:81], v[122:125], v[224:227], v[78:81]
	s_waitcnt lgkmcnt(4)
	v_mfma_f32_16x16x32_f16 v[70:73], v[122:125], v[228:231], v[70:73]
	s_waitcnt vmcnt(13)
	v_mfma_f32_16x16x32_f16 v[54:57], v[156:159], v[176:179], v[54:57]
	v_mfma_f32_16x16x32_f16 v[74:77], v[156:159], v[220:223], v[74:77]
	v_mfma_f32_16x16x32_f16 v[82:85], v[156:159], v[224:227], v[82:85]
	v_mfma_f32_16x16x32_f16 v[62:65], v[156:159], v[228:231], v[62:65]
	s_waitcnt vmcnt(12)
	v_mfma_f32_16x16x32_f16 v[38:41], v[180:183], v[176:179], v[38:41]
	v_mfma_f32_16x16x32_f16 v[42:45], v[180:183], v[220:223], v[42:45]
	buffer_load_dwordx4 v[122:125], v147, s[16:19], s8 offen
	buffer_load_dwordx4 v[156:159], v148, s[16:19], s8 offen
	buffer_load_dwordx4 v[176:179], v149, s[16:19], s8 offen
	buffer_load_dwordx4 v[220:223], v150, s[16:19], s8 offen
	v_mfma_f32_16x16x32_f16 v[50:53], v[94:97], v[228:231], v[50:53]
	v_mfma_f32_16x16x32_f16 v[46:49], v[180:183], v[224:227], v[46:49]
	v_mfma_f32_16x16x32_f16 v[34:37], v[180:183], v[228:231], v[34:37]
	v_mfma_f32_16x16x32_f16 v[172:175], v[94:97], v[224:227], v[172:175]
	v_add_u32_e32 v117, s77, v100
	ds_read_b128 v[94:97], v117
	ds_read_b128 v[180:183], v117 offset:16384
	ds_read_b128 v[224:227], v117 offset:32768
	ds_read_b128 v[228:231], v117 offset:49152
	s_add_i32 s8, s22, s46
	s_waitcnt vmcnt(15) lgkmcnt(7)
	v_mfma_f32_16x16x32_f16 v[164:167], v[90:93], v[204:207], v[164:167]
	s_waitcnt lgkmcnt(6)
	v_mfma_f32_16x16x32_f16 v[168:171], v[90:93], v[208:211], v[168:171]
	s_waitcnt lgkmcnt(5)
	v_mfma_f32_16x16x32_f16 v[172:175], v[90:93], v[212:215], v[172:175]
	s_waitcnt lgkmcnt(4)
	v_mfma_f32_16x16x32_f16 v[90:93], v[90:93], v[216:219], v[50:53]
	s_waitcnt vmcnt(14)
	v_mfma_f32_16x16x32_f16 v[232:235], v[188:191], v[204:207], v[58:61]
	v_mfma_f32_16x16x32_f16 v[66:69], v[188:191], v[208:211], v[66:69]
	v_mfma_f32_16x16x32_f16 v[78:81], v[188:191], v[212:215], v[78:81]
	v_mfma_f32_16x16x32_f16 v[70:73], v[188:191], v[216:219], v[70:73]
	s_waitcnt vmcnt(13)
	v_mfma_f32_16x16x32_f16 v[188:191], v[192:195], v[204:207], v[54:57]
	v_mfma_f32_16x16x32_f16 v[74:77], v[192:195], v[208:211], v[74:77]
	v_mfma_f32_16x16x32_f16 v[82:85], v[192:195], v[212:215], v[82:85]
	v_mfma_f32_16x16x32_f16 v[62:65], v[192:195], v[216:219], v[62:65]
	s_waitcnt vmcnt(12)
	v_mfma_f32_16x16x32_f16 v[192:195], v[196:199], v[204:207], v[38:41]
	buffer_load_dwordx4 v[58:61], v147, s[16:19], s8 offen
	buffer_load_dwordx4 v[54:57], v148, s[16:19], s8 offen
	buffer_load_dwordx4 v[50:53], v149, s[16:19], s8 offen
	buffer_load_dwordx4 v[38:41], v150, s[16:19], s8 offen
	v_mfma_f32_16x16x32_f16 v[42:45], v[196:199], v[208:211], v[42:45]
	v_mfma_f32_16x16x32_f16 v[46:49], v[196:199], v[212:215], v[46:49]
	v_mfma_f32_16x16x32_f16 v[196:199], v[196:199], v[216:219], v[34:37]
	v_add_u32_e32 v117, s78, v98
	ds_read_b128 v[204:207], v117
	ds_read_b128 v[208:211], v117 offset:16384
	ds_read_b128 v[212:215], v117 offset:32768
	ds_read_b128 v[216:219], v117 offset:49152
	s_add_i32 s8, s22, s47
	s_waitcnt vmcnt(15) lgkmcnt(7)
	v_mfma_f32_16x16x32_f16 v[164:167], v[86:89], v[94:97], v[164:167]
	s_waitcnt lgkmcnt(6)
	v_mfma_f32_16x16x32_f16 v[168:171], v[86:89], v[180:183], v[168:171]
	s_waitcnt lgkmcnt(5)
	v_mfma_f32_16x16x32_f16 v[172:175], v[86:89], v[224:227], v[172:175]
	s_waitcnt lgkmcnt(4)
	v_mfma_f32_16x16x32_f16 v[86:89], v[86:89], v[228:231], v[90:93]
	s_waitcnt vmcnt(14)
	v_mfma_f32_16x16x32_f16 v[232:235], v[140:143], v[94:97], v[232:235]
	v_mfma_f32_16x16x32_f16 v[66:69], v[140:143], v[180:183], v[66:69]
	v_mfma_f32_16x16x32_f16 v[236:239], v[140:143], v[224:227], v[78:81]
	v_mfma_f32_16x16x32_f16 v[70:73], v[140:143], v[228:231], v[70:73]
	s_waitcnt vmcnt(13)
	v_mfma_f32_16x16x32_f16 v[140:143], v[152:155], v[94:97], v[188:191]
	v_mfma_f32_16x16x32_f16 v[74:77], v[152:155], v[180:183], v[74:77]
	v_mfma_f32_16x16x32_f16 v[82:85], v[152:155], v[224:227], v[82:85]
	v_mfma_f32_16x16x32_f16 v[62:65], v[152:155], v[228:231], v[62:65]
	s_waitcnt vmcnt(12)
	v_mfma_f32_16x16x32_f16 v[152:155], v[160:163], v[94:97], v[192:195]
	buffer_load_dwordx4 v[94:97], v147, s[16:19], s8 offen
	buffer_load_dwordx4 v[90:93], v148, s[16:19], s8 offen
	buffer_load_dwordx4 v[78:81], v149, s[16:19], s8 offen
	buffer_load_dwordx4 v[34:37], v150, s[16:19], s8 offen
	v_mfma_f32_16x16x32_f16 v[42:45], v[160:163], v[180:183], v[42:45]
	v_mfma_f32_16x16x32_f16 v[46:49], v[160:163], v[224:227], v[46:49]
	v_mfma_f32_16x16x32_f16 v[160:163], v[160:163], v[228:231], v[196:199]
	v_add_u32_e32 v117, s79, v100
	ds_read_b128 v[180:183], v117
	ds_read_b128 v[188:191], v117 offset:16384
	ds_read_b128 v[192:195], v117 offset:32768
	ds_read_b128 v[196:199], v117 offset:49152
	s_add_i32 s8, s22, s48
	s_waitcnt vmcnt(15) lgkmcnt(7)
	v_mfma_f32_16x16x32_f16 v[164:167], v[126:129], v[204:207], v[164:167]
	s_waitcnt lgkmcnt(6)
	v_mfma_f32_16x16x32_f16 v[168:171], v[126:129], v[208:211], v[168:171]
	s_waitcnt lgkmcnt(5)
	v_mfma_f32_16x16x32_f16 v[172:175], v[126:129], v[212:215], v[172:175]
	s_waitcnt lgkmcnt(4)
	v_mfma_f32_16x16x32_f16 v[86:89], v[126:129], v[216:219], v[86:89]
	s_waitcnt vmcnt(14)
	v_mfma_f32_16x16x32_f16 v[126:129], v[136:139], v[204:207], v[232:235]
	v_mfma_f32_16x16x32_f16 v[66:69], v[136:139], v[208:211], v[66:69]
	v_mfma_f32_16x16x32_f16 v[224:227], v[136:139], v[212:215], v[236:239]
	v_mfma_f32_16x16x32_f16 v[136:139], v[136:139], v[216:219], v[70:73]
	s_waitcnt vmcnt(13)
	v_mfma_f32_16x16x32_f16 v[140:143], v[184:187], v[204:207], v[140:143]
	v_mfma_f32_16x16x32_f16 v[74:77], v[184:187], v[208:211], v[74:77]
	v_mfma_f32_16x16x32_f16 v[228:231], v[184:187], v[212:215], v[82:85]
	v_mfma_f32_16x16x32_f16 v[184:187], v[184:187], v[216:219], v[62:65]
	s_waitcnt vmcnt(12)
	v_mfma_f32_16x16x32_f16 v[152:155], v[200:203], v[204:207], v[152:155]
	v_mfma_f32_16x16x32_f16 v[204:207], v[200:203], v[208:211], v[42:45]
	buffer_load_dwordx4 v[82:85], v147, s[16:19], s8 offen
	buffer_load_dwordx4 v[70:73], v148, s[16:19], s8 offen
	buffer_load_dwordx4 v[62:65], v149, s[16:19], s8 offen
	buffer_load_dwordx4 v[42:45], v150, s[16:19], s8 offen
	v_mfma_f32_16x16x32_f16 v[46:49], v[200:203], v[212:215], v[46:49]
	v_mfma_f32_16x16x32_f16 v[160:163], v[200:203], v[216:219], v[160:163]
	v_add_u32_e32 v0, 0x1ac00, v104
	ds_read_b128 v[240:243], v0
	ds_read_b128 v[244:247], v0 offset:16
	s_waitcnt vmcnt(12) lgkmcnt(5)
	v_mfma_f32_16x16x32_f16 v[164:167], v[122:125], v[180:183], v[164:167]
	v_mfma_f32_16x16x32_f16 v[126:129], v[156:159], v[180:183], v[126:129]
	v_mfma_f32_16x16x32_f16 v[140:143], v[176:179], v[180:183], v[140:143]
	v_mfma_f32_16x16x32_f16 v[152:155], v[220:223], v[180:183], v[152:155]
	s_waitcnt lgkmcnt(4)
	v_mfma_f32_16x16x32_f16 v[168:171], v[122:125], v[188:191], v[168:171]
	v_mfma_f32_16x16x32_f16 v[208:211], v[156:159], v[188:191], v[66:69]
	v_mfma_f32_16x16x32_f16 v[212:215], v[176:179], v[188:191], v[74:77]
	v_mfma_f32_16x16x32_f16 v[204:207], v[220:223], v[188:191], v[204:207]
	s_waitcnt lgkmcnt(3)
	v_mfma_f32_16x16x32_f16 v[172:175], v[122:125], v[192:195], v[172:175]
	v_cvt_pk_f16_f32 v232, v164, v165
	v_cvt_pk_f16_f32 v233, v166, v167
	v_pk_max_f16 v232, v232, 0
	v_pk_max_f16 v233, v233, 0
	v_mfma_f32_16x16x32_f16 v[224:227], v[156:159], v[192:195], v[224:227]
	v_cvt_pk_f16_f32 v234, v126, v127
	v_cvt_pk_f16_f32 v235, v128, v129
	v_pk_max_f16 v234, v234, 0
	v_pk_max_f16 v235, v235, 0
	v_mfma_f32_16x16x32_f16 v[228:231], v[176:179], v[192:195], v[228:231]
	v_cvt_pk_f16_f32 v236, v140, v141
	v_cvt_pk_f16_f32 v237, v142, v143
	v_pk_max_f16 v236, v236, 0
	v_pk_max_f16 v237, v237, 0
	v_mfma_f32_16x16x32_f16 v[216:219], v[220:223], v[192:195], v[46:49]
	v_cvt_pk_f16_f32 v238, v152, v153
	v_cvt_pk_f16_f32 v239, v154, v155
	v_pk_max_f16 v238, v238, 0
	v_pk_max_f16 v239, v239, 0
	s_waitcnt lgkmcnt(2)
	v_mfma_f32_16x16x32_f16 v[200:203], v[122:125], v[196:199], v[86:89]
	v_cvt_pk_f16_f32 v180, v168, v169
	v_cvt_pk_f16_f32 v181, v170, v171
	v_pk_max_f16 v180, v180, 0
	v_pk_max_f16 v181, v181, 0
	s_add_i32 s8, s22, s49
	buffer_load_dwordx4 v[86:89], v147, s[16:19], s8 offen
	buffer_load_dwordx4 v[74:77], v148, s[16:19], s8 offen
	buffer_load_dwordx4 v[66:69], v149, s[16:19], s8 offen
	buffer_load_dwordx4 v[46:49], v150, s[16:19], s8 offen
	v_mfma_f32_16x16x32_f16 v[136:139], v[156:159], v[196:199], v[136:139]
	v_cvt_pk_f16_f32 v182, v208, v209
	v_cvt_pk_f16_f32 v183, v210, v211
	v_pk_max_f16 v182, v182, 0
	v_pk_max_f16 v183, v183, 0
	s_waitcnt lgkmcnt(1)
	v_mfma_f32_16x16x32_f16 v[252:255], v[240:243], v[232:235], 0
	v_cvt_pk_f16_f32 v232, v172, v173
	v_cvt_pk_f16_f32 v233, v174, v175
	v_pk_max_f16 v232, v232, 0
	v_pk_max_f16 v233, v233, 0
	v_mfma_f32_16x16x32_f16 v[184:187], v[176:179], v[196:199], v[184:187]
	v_cvt_pk_f16_f32 v188, v212, v213
	v_cvt_pk_f16_f32 v189, v214, v215
	v_pk_max_f16 v188, v188, 0
	v_pk_max_f16 v189, v189, 0
	s_waitcnt lgkmcnt(0)
	v_mfma_f32_16x16x32_f16 v[252:255], v[244:247], v[236:239], v[252:255]
	ds_read_u16 v102, v114
	ds_read_u16 v103, v114 offset:512
	ds_read_u16 v115, v114 offset:1024
	ds_read_u16 v116, v114 offset:1536
	v_cvt_pk_f16_f32 v234, v224, v225
	v_cvt_pk_f16_f32 v235, v226, v227
	v_pk_max_f16 v234, v234, 0
	v_pk_max_f16 v235, v235, 0
	v_mfma_f32_16x16x32_f16 v[160:163], v[220:223], v[196:199], v[160:163]
	v_cvt_pk_f16_f32 v190, v204, v205
	v_cvt_pk_f16_f32 v191, v206, v207
	v_pk_max_f16 v190, v190, 0
	v_pk_max_f16 v191, v191, 0
	v_mfma_f32_16x16x32_f16 v[192:195], v[240:243], v[180:183], 0
	v_cvt_pk_f16_f32 v236, v228, v229
	v_cvt_pk_f16_f32 v237, v230, v231
	v_pk_max_f16 v236, v236, 0
	v_pk_max_f16 v237, v237, 0
	v_mfma_f32_16x16x32_f16 v[192:195], v[244:247], v[188:191], v[192:195]
	v_cvt_pk_f16_f32 v238, v216, v217
	v_cvt_pk_f16_f32 v239, v218, v219
	v_pk_max_f16 v238, v238, 0
	v_pk_max_f16 v239, v239, 0
	v_cvt_pk_f16_f32 v180, v200, v201
	v_cvt_pk_f16_f32 v181, v202, v203
	v_pk_max_f16 v180, v180, 0
	v_pk_max_f16 v181, v181, 0
	v_mfma_f32_16x16x32_f16 v[196:199], v[240:243], v[232:235], 0
	v_cvt_pk_f16_f32 v182, v136, v137
	v_cvt_pk_f16_f32 v183, v138, v139
	v_pk_max_f16 v182, v182, 0
	v_pk_max_f16 v183, v183, 0
	v_mfma_f32_16x16x32_f16 v[196:199], v[244:247], v[236:239], v[196:199]
	v_cvt_pk_f16_f32 v188, v184, v185
	v_cvt_pk_f16_f32 v189, v186, v187
	v_pk_max_f16 v188, v188, 0
	v_pk_max_f16 v189, v189, 0
	v_cvt_pk_f16_f32 v190, v160, v161
	v_cvt_pk_f16_f32 v191, v162, v163
	v_pk_max_f16 v190, v190, 0
	v_pk_max_f16 v191, v191, 0
	v_mfma_f32_16x16x32_f16 v[122:125], v[240:243], v[180:183], 0
	s_nop 0
	v_mfma_f32_16x16x32_f16 v[122:125], v[244:247], v[188:191], v[122:125]
	v_add_u32_e32 v145, 0x12c00, v105
	ds_read_b128 v[240:243], v145 offset:2048
	ds_read_b128 v[244:247], v145 offset:2064
	ds_read_b128 v[248:251], v145 offset:2080
	s_load_dword s30, s[12:13], 0x0
	v_cndmask_b32_e64 v0, v252, v192, s[2:3]
	ds_read_b128 v[252:255], v145 offset:2096
	v_cndmask_b32_e64 v0, v0, v196, s[0:1]
	v_cndmask_b32_e64 v0, v0, v122, s[26:27]
	ds_write_b32 v112, v0
	s_waitcnt vmcnt(16)
	v_cndmask_b32_e64 v1, v30, v134, s[0:1]
	v_bfi_b32 v30, s10, v1, v30
	v_perm_b32 v1, v22, v134, s24
	v_cndmask_b32_e64 v22, v22, v1, s[0:1]
	v_bfi_b32 v1, s10, v135, v18
	v_perm_b32 v121, v10, v135, s24
	v_cndmask_b32_e64 v18, v18, v1, s[0:1]
	v_cndmask_b32_e64 v10, v10, v121, s[0:1]
	s_add_i32 s22, s22, 0x80000
	s_add_i32 s11, s11, 1
	s_add_u32 s12, s12, 4
	s_addc_u32 s13, s13, 0
	v_add_u32_e32 v104, 0x400, v104
	v_add_u32_e32 v105, 0x800, v105
	v_add_u32_e32 v114, 2, v114
	s_cmp_eq_u32 s22, 0x898000
	s_waitcnt lgkmcnt(0)
	s_barrier
	ds_read_b128 v[232:235], v113
	ds_read_b128 v[236:239], v113 offset:1024
	s_waitcnt lgkmcnt(0)
	v_add_f32_e32 v0, v232, v233
	v_add_f32_e32 v1, v234, v235
	v_add_f32_e32 v121, v236, v237
	v_add_f32_e32 v144, v238, v239
	v_add_f32_e32 v0, v0, v1
	v_add_f32_e32 v121, v121, v144
	v_add_f32_e32 v0, v0, v121
	v_add_f32_e32 v0, s30, v0
	v_cvt_f16_f32_e32 v1, v0
	v_cvt_f16_f32_e32 v121, v0
	ds_write_b32 v106, v0
	v_add_u32_e32 v106, 4, v106
	v_permlane16_swap_b32_e32 v1, v121
	s_cbranch_scc0 .LBB1_4
